# baseline (speedup 1.0000x reference)
.Lp_main:
	s_load_dwordx2 s[10:11], s[0:1], 0x0
	s_load_dwordx4 s[12:15], s[0:1], 0x10
	s_load_dwordx2 s[16:17], s[0:1], 0x20
	s_load_dwordx4 s[20:23], s[0:1], 0x28
	v_readfirstlane_b32 s3, v0
	v_and_b32_e32 v154, 63, v0
	v_lshrrev_b32_e32 v155, 5, v154
	v_lshlrev_b32_e32 v156, 4, v0
	v_lshlrev_b32_e32 v157, 4, v154
	v_lshlrev_b32_e32 v158, 8, v1
	v_lshl_add_u32 v158, v155, 5, v158
	v_lshlrev_b32_e32 v159, 4, v155
	v_lshrrev_b32_e32 v160, 3, v0
	v_lshlrev_b32_e32 v160, 12, v160
	v_and_b32_e32 v161, 7, v0
	v_lshl_add_u32 v160, v161, 4, v160
	s_lshr_b32 s41, s2, 3
	s_and_b32 s42, s2, 7
	s_lshl_b32 s24, s42, 2
	s_bfe_u32 s25, s2, 0x20003
	s_add_u32 s24, s24, s25
	s_lshr_b32 s25, s2, 5
	s_lshr_b32 s26, s3, 6
	s_lshl_b32 s27, s25, 2
	s_add_u32 s27, s27, s26
	s_mov_b32 s4, 0x4038aa3b
	s_mov_b32 s5, s4
	s_lshl_b32 s40, s26, 6
	s_waitcnt lgkmcnt(0)
	s_lshl_b32 s28, s24, 15
	s_add_u32 s28, s28, 0x1000
	s_add_u32 s10, s10, s28
	s_addc_u32 s11, s11, 0
	s_lshl_b32 s34, s41, 17
	s_lshl_b32 s35, s42, 9
	s_add_u32 s34, s34, s35
	s_add_u32 s34, s14, s34
	s_addc_u32 s35, s15, 0
	s_lshl_b32 s28, s27, 13
	s_add_u32 s28, s8, s28
	s_addc_u32 s29, s9, 0
	s_lshl_b32 s30, s27, 7
	s_add_u32 s30, s12, s30
	s_addc_u32 s31, s13, 0
	global_load_dwordx4 v[2:5], v156, s[10:11] offset:-4096
	global_load_dwordx4 v[6:9], v156, s[10:11] offset:0
	s_add_u32 s10, s10, 0x2000
	s_addc_u32 s11, s11, 0
	global_load_dwordx4 v[10:13], v156, s[10:11] offset:-4096
	global_load_dwordx4 v[14:17], v156, s[10:11] offset:0
	s_add_u32 s10, s10, 0x2000
	s_addc_u32 s11, s11, 0
	global_load_dwordx4 v[18:21], v156, s[10:11] offset:-4096
	global_load_dwordx4 v[22:25], v156, s[10:11] offset:0
	s_add_u32 s10, s10, 0x2000
	s_addc_u32 s11, s11, 0
	global_load_dwordx4 v[26:29], v156, s[10:11] offset:-4096
	global_load_dwordx4 v[30:33], v156, s[10:11] offset:0
	global_load_dwordx4 v[34:37], v158, s[28:29] offset:0
	global_load_dwordx4 v[38:41], v158, s[28:29] offset:16
	global_load_dwordx4 v[42:45], v158, s[28:29] offset:64
	global_load_dwordx4 v[46:49], v158, s[28:29] offset:80
	global_load_dwordx4 v[50:53], v158, s[28:29] offset:128
	global_load_dwordx4 v[54:57], v158, s[28:29] offset:144
	global_load_dwordx4 v[58:61], v158, s[28:29] offset:192
	global_load_dwordx4 v[62:65], v158, s[28:29] offset:208
	global_load_dwordx4 v[66:69], v159, s[30:31] offset:0
	global_load_dwordx4 v[70:73], v159, s[30:31] offset:32
	global_load_dwordx4 v[74:77], v159, s[30:31] offset:64
	global_load_dwordx4 v[78:81], v159, s[30:31] offset:96
	v_bfe_u32 v163, v0, 1, 3
	v_mul_u32_u24_e32 v163, 0x210, v163
	v_lshrrev_b32_e32 v164, 4, v0
	v_lshl_add_u32 v163, v164, 4, v163
	v_and_b32_e32 v164, 1, v0
	v_lshl_add_u32 v163, v164, 3, v163
	v_lshrrev_b32_e32 v164, 3, v0
	v_mul_u32_u24_e32 v164, 0x110, v164
	v_lshl_add_u32 v164, v161, 3, v164
	v_add_u32_e32 v164, 0x4200, v164
	v_mul_u32_u24_e32 v165, 0x210, v155
	v_lshl_add_u32 v165, v1, 4, v165
	v_mul_u32_u24_e32 v166, 0x110, v1
	v_lshl_add_u32 v166, v155, 4, v166
	v_add_u32_e32 v166, s40, v166
	v_add_u32_e32 v166, 0x4200, v166
	v_mul_u32_u24_e32 v167, 0x880, v155
	v_lshl_add_u32 v167, v1, 1, v167
	v_add_u32_e32 v167, s40, v167
	v_add_u32_e32 v167, 0x4200, v167
	s_lshl_b32 s32, s24, 18
	s_lshl_b32 s33, s27, 11
	s_add_u32 s32, s32, s33
	s_add_u32 s32, s16, s32
	s_addc_u32 s33, s17, 0
	s_lshl_b32 s36, s41, 16
	s_lshl_b32 s37, s42, 13
	s_add_u32 s36, s36, s37
	s_lshl_b32 s37, s26, 11
	s_add_u32 s36, s36, s37
	s_add_u32 s36, s20, s36
	s_addc_u32 s37, s21, 0
	s_lshl_b32 s38, s42, 18
	s_lshl_b32 s39, s26, 16
	s_add_u32 s38, s38, s39
	s_lshl_b32 s39, s41, 11
	s_add_u32 s38, s38, s39
	s_add_u32 s38, s22, s38
	s_addc_u32 s39, s23, 0
	s_waitcnt vmcnt(19)
	v_cvt_pk_f16_f32 v2, v2, v3
	v_cvt_pk_f16_f32 v3, v4, v5
	ds_write_b64 v163, v[2:3] offset:0
	s_waitcnt vmcnt(18)
	v_cvt_pk_f16_f32 v6, v6, v7
	v_cvt_pk_f16_f32 v7, v8, v9
	ds_write_b64 v163, v[6:7] offset:256
	s_waitcnt vmcnt(17)
	v_cvt_pk_f16_f32 v10, v10, v11
	v_cvt_pk_f16_f32 v11, v12, v13
	ds_write_b64 v163, v[10:11] offset:4224
	s_waitcnt vmcnt(16)
	v_cvt_pk_f16_f32 v14, v14, v15
	v_cvt_pk_f16_f32 v15, v16, v17
	ds_write_b64 v163, v[14:15] offset:4480
	s_waitcnt vmcnt(15)
	v_cvt_pk_f16_f32 v18, v18, v19
	v_cvt_pk_f16_f32 v19, v20, v21
	ds_write_b64 v163, v[18:19] offset:8448
	s_waitcnt vmcnt(14)
	v_cvt_pk_f16_f32 v22, v22, v23
	v_cvt_pk_f16_f32 v23, v24, v25
	ds_write_b64 v163, v[22:23] offset:8704
	s_waitcnt vmcnt(13)
	v_cvt_pk_f16_f32 v26, v26, v27
	v_cvt_pk_f16_f32 v27, v28, v29
	ds_write_b64 v163, v[26:27] offset:12672
	s_waitcnt vmcnt(12)
	v_cvt_pk_f16_f32 v30, v30, v31
	v_cvt_pk_f16_f32 v31, v32, v33
	ds_write_b64 v163, v[30:31] offset:12928
	s_waitcnt lgkmcnt(0)
	s_barrier
	ds_read_b128 v[2:5], v165 offset:0
	ds_read_b128 v[6:9], v165 offset:1056
	ds_read_b128 v[10:13], v165 offset:2112
	ds_read_b128 v[14:17], v165 offset:3168
	ds_read_b128 v[18:21], v165 offset:4224
	ds_read_b128 v[22:25], v165 offset:5280
	ds_read_b128 v[26:29], v165 offset:6336
	ds_read_b128 v[30:33], v165 offset:7392
	s_waitcnt vmcnt(4)
	v_cvt_pk_f16_f32 v82, v34, v35
	v_cvt_pk_f16_f32 v83, v36, v37
	v_cvt_pk_f16_f32 v84, v38, v39
	v_cvt_pk_f16_f32 v85, v40, v41
	v_cvt_pk_f16_f32 v86, v42, v43
	v_cvt_pk_f16_f32 v87, v44, v45
	v_cvt_pk_f16_f32 v88, v46, v47
	v_cvt_pk_f16_f32 v89, v48, v49
	v_cvt_pk_f16_f32 v90, v50, v51
	v_cvt_pk_f16_f32 v91, v52, v53
	v_cvt_pk_f16_f32 v92, v54, v55
	v_cvt_pk_f16_f32 v93, v56, v57
	v_cvt_pk_f16_f32 v94, v58, v59
	v_cvt_pk_f16_f32 v95, v60, v61
	v_cvt_pk_f16_f32 v96, v62, v63
	v_cvt_pk_f16_f32 v97, v64, v65
	ds_read_b128 v[34:37], v165 offset:8448
	ds_read_b128 v[38:41], v165 offset:9504
	ds_read_b128 v[42:45], v165 offset:10560
	ds_read_b128 v[46:49], v165 offset:11616
	s_waitcnt vmcnt(0)
	v_pk_mul_f32 v[66:67], v[66:67], s[4:5] op_sel_hi:[1,0]
	v_pk_mul_f32 v[68:69], v[68:69], s[4:5] op_sel_hi:[1,0]
	v_pk_mul_f32 v[70:71], v[70:71], s[4:5] op_sel_hi:[1,0]
	v_pk_mul_f32 v[72:73], v[72:73], s[4:5] op_sel_hi:[1,0]
	v_pk_mul_f32 v[74:75], v[74:75], s[4:5] op_sel_hi:[1,0]
	v_pk_mul_f32 v[76:77], v[76:77], s[4:5] op_sel_hi:[1,0]
	v_pk_mul_f32 v[78:79], v[78:79], s[4:5] op_sel_hi:[1,0]
	v_pk_mul_f32 v[80:81], v[80:81], s[4:5] op_sel_hi:[1,0]
	global_load_dwordx4 v[168:171], v160, s[34:35] offset:0
	global_load_dwordx4 v[172:175], v160, s[34:35] offset:128
	global_load_dwordx4 v[176:179], v160, s[34:35] offset:256
	global_load_dwordx4 v[180:183], v160, s[34:35] offset:384
	s_waitcnt lgkmcnt(8)
	v_mfma_f32_32x32x16_f16 v[98:113], v[82:85], v[2:5], 0
	v_mfma_f32_32x32x16_f16 v[98:113], v[86:89], v[6:9], v[98:113]
	v_mfma_f32_32x32x16_f16 v[98:113], v[90:93], v[10:13], v[98:113]
	v_mfma_f32_32x32x16_f16 v[98:113], v[94:97], v[14:17], v[98:113]
	ds_read_b128 v[50:53], v165 offset:12672
	ds_read_b128 v[54:57], v165 offset:13728
	ds_read_b128 v[58:61], v165 offset:14784
	ds_read_b128 v[62:65], v165 offset:15840
	s_waitcnt lgkmcnt(8)
	v_mfma_f32_32x32x16_f16 v[114:129], v[82:85], v[18:21], 0
	v_mfma_f32_32x32x16_f16 v[114:129], v[86:89], v[22:25], v[114:129]
	v_mfma_f32_32x32x16_f16 v[114:129], v[90:93], v[26:29], v[114:129]
	v_mfma_f32_32x32x16_f16 v[114:129], v[94:97], v[30:33], v[114:129]
	s_nop 7
	v_pk_fma_f32 v[130:131], v[98:99], s[4:5], v[66:67] op_sel_hi:[1,0,1]
	v_pk_fma_f32 v[132:133], v[100:101], s[4:5], v[68:69] op_sel_hi:[1,0,1]
	v_pk_fma_f32 v[134:135], v[102:103], s[4:5], v[70:71] op_sel_hi:[1,0,1]
	v_pk_fma_f32 v[136:137], v[104:105], s[4:5], v[72:73] op_sel_hi:[1,0,1]
	v_pk_fma_f32 v[138:139], v[106:107], s[4:5], v[74:75] op_sel_hi:[1,0,1]
	v_pk_fma_f32 v[140:141], v[108:109], s[4:5], v[76:77] op_sel_hi:[1,0,1]
	v_pk_fma_f32 v[142:143], v[110:111], s[4:5], v[78:79] op_sel_hi:[1,0,1]
	v_pk_fma_f32 v[144:145], v[112:113], s[4:5], v[80:81] op_sel_hi:[1,0,1]
	v_exp_f32_e32 v130, v130
	v_exp_f32_e32 v131, v131
	v_exp_f32_e32 v132, v132
	v_exp_f32_e32 v133, v133
	v_exp_f32_e32 v134, v134
	v_exp_f32_e32 v135, v135
	v_exp_f32_e32 v136, v136
	v_exp_f32_e32 v137, v137
	v_exp_f32_e32 v138, v138
	v_exp_f32_e32 v139, v139
	v_exp_f32_e32 v140, v140
	v_exp_f32_e32 v141, v141
	v_exp_f32_e32 v142, v142
	v_exp_f32_e32 v143, v143
	v_exp_f32_e32 v144, v144
	v_exp_f32_e32 v145, v145
	v_pk_add_f32 v[130:131], v[130:131], 1.0 op_sel_hi:[1,0]
	v_pk_add_f32 v[132:133], v[132:133], 1.0 op_sel_hi:[1,0]
	v_pk_add_f32 v[134:135], v[134:135], 1.0 op_sel_hi:[1,0]
	v_pk_add_f32 v[136:137], v[136:137], 1.0 op_sel_hi:[1,0]
	v_pk_add_f32 v[138:139], v[138:139], 1.0 op_sel_hi:[1,0]
	v_pk_add_f32 v[140:141], v[140:141], 1.0 op_sel_hi:[1,0]
	v_pk_add_f32 v[142:143], v[142:143], 1.0 op_sel_hi:[1,0]
	v_pk_add_f32 v[144:145], v[144:145], 1.0 op_sel_hi:[1,0]
	v_rcp_f32_e32 v130, v130
	v_rcp_f32_e32 v131, v131
	v_rcp_f32_e32 v132, v132
	v_rcp_f32_e32 v133, v133
	v_rcp_f32_e32 v134, v134
	v_rcp_f32_e32 v135, v135
	v_rcp_f32_e32 v136, v136
	v_rcp_f32_e32 v137, v137
	v_rcp_f32_e32 v138, v138
	v_rcp_f32_e32 v139, v139
	v_rcp_f32_e32 v140, v140
	v_rcp_f32_e32 v141, v141
	v_rcp_f32_e32 v142, v142
	v_rcp_f32_e32 v143, v143
	v_rcp_f32_e32 v144, v144
	v_rcp_f32_e32 v145, v145
	v_pk_fma_f32 v[130:131], v[130:131], 2.0, 1.0 op_sel_hi:[1,0,0] neg_lo:[1,0,0] neg_hi:[1,0,0]
	v_pk_fma_f32 v[132:133], v[132:133], 2.0, 1.0 op_sel_hi:[1,0,0] neg_lo:[1,0,0] neg_hi:[1,0,0]
	v_pk_fma_f32 v[134:135], v[134:135], 2.0, 1.0 op_sel_hi:[1,0,0] neg_lo:[1,0,0] neg_hi:[1,0,0]
	v_pk_fma_f32 v[136:137], v[136:137], 2.0, 1.0 op_sel_hi:[1,0,0] neg_lo:[1,0,0] neg_hi:[1,0,0]
	v_pk_fma_f32 v[138:139], v[138:139], 2.0, 1.0 op_sel_hi:[1,0,0] neg_lo:[1,0,0] neg_hi:[1,0,0]
	v_pk_fma_f32 v[140:141], v[140:141], 2.0, 1.0 op_sel_hi:[1,0,0] neg_lo:[1,0,0] neg_hi:[1,0,0]
	v_pk_fma_f32 v[142:143], v[142:143], 2.0, 1.0 op_sel_hi:[1,0,0] neg_lo:[1,0,0] neg_hi:[1,0,0]
	v_pk_fma_f32 v[144:145], v[144:145], 2.0, 1.0 op_sel_hi:[1,0,0] neg_lo:[1,0,0] neg_hi:[1,0,0]
	v_cvt_pk_f16_f32 v146, v130, v131
	v_cvt_pk_f16_f32 v147, v132, v133
	v_cvt_pk_f16_f32 v148, v134, v135
	v_cvt_pk_f16_f32 v149, v136, v137
	v_cvt_pk_f16_f32 v150, v138, v139
	v_cvt_pk_f16_f32 v151, v140, v141
	v_cvt_pk_f16_f32 v152, v142, v143
	v_cvt_pk_f16_f32 v153, v144, v145
	s_nop 1
	v_permlane32_swap_b32_e32 v146, v148
	v_permlane32_swap_b32_e32 v147, v149
	v_permlane32_swap_b32_e32 v150, v152
	v_permlane32_swap_b32_e32 v151, v153
	global_store_dwordx4 v157, v[146:149], s[32:33] sc1
	global_store_dwordx4 v157, v[150:153], s[32:33] offset:1024 sc1
	s_add_u32 s32, s32, 0x10000
	s_addc_u32 s33, s33, 0
	s_waitcnt lgkmcnt(4)
	v_mfma_f32_32x32x16_f16 v[98:113], v[82:85], v[34:37], 0
	v_mfma_f32_32x32x16_f16 v[98:113], v[86:89], v[38:41], v[98:113]
	v_mfma_f32_32x32x16_f16 v[98:113], v[90:93], v[42:45], v[98:113]
	v_mfma_f32_32x32x16_f16 v[98:113], v[94:97], v[46:49], v[98:113]
	v_pk_fma_f32 v[130:131], v[114:115], s[4:5], v[66:67] op_sel_hi:[1,0,1]
	v_pk_fma_f32 v[132:133], v[116:117], s[4:5], v[68:69] op_sel_hi:[1,0,1]
	v_pk_fma_f32 v[134:135], v[118:119], s[4:5], v[70:71] op_sel_hi:[1,0,1]
	v_pk_fma_f32 v[136:137], v[120:121], s[4:5], v[72:73] op_sel_hi:[1,0,1]
	v_pk_fma_f32 v[138:139], v[122:123], s[4:5], v[74:75] op_sel_hi:[1,0,1]
	v_pk_fma_f32 v[140:141], v[124:125], s[4:5], v[76:77] op_sel_hi:[1,0,1]
	v_pk_fma_f32 v[142:143], v[126:127], s[4:5], v[78:79] op_sel_hi:[1,0,1]
	v_pk_fma_f32 v[144:145], v[128:129], s[4:5], v[80:81] op_sel_hi:[1,0,1]
	v_exp_f32_e32 v130, v130
	v_exp_f32_e32 v131, v131
	v_exp_f32_e32 v132, v132
	v_exp_f32_e32 v133, v133
	v_exp_f32_e32 v134, v134
	v_exp_f32_e32 v135, v135
	v_exp_f32_e32 v136, v136
	v_exp_f32_e32 v137, v137
	v_exp_f32_e32 v138, v138
	v_exp_f32_e32 v139, v139
	v_exp_f32_e32 v140, v140
	v_exp_f32_e32 v141, v141
	v_exp_f32_e32 v142, v142
	v_exp_f32_e32 v143, v143
	v_exp_f32_e32 v144, v144
	v_exp_f32_e32 v145, v145
	v_pk_add_f32 v[130:131], v[130:131], 1.0 op_sel_hi:[1,0]
	v_pk_add_f32 v[132:133], v[132:133], 1.0 op_sel_hi:[1,0]
	v_pk_add_f32 v[134:135], v[134:135], 1.0 op_sel_hi:[1,0]
	v_pk_add_f32 v[136:137], v[136:137], 1.0 op_sel_hi:[1,0]
	v_pk_add_f32 v[138:139], v[138:139], 1.0 op_sel_hi:[1,0]
	v_pk_add_f32 v[140:141], v[140:141], 1.0 op_sel_hi:[1,0]
	v_pk_add_f32 v[142:143], v[142:143], 1.0 op_sel_hi:[1,0]
	v_pk_add_f32 v[144:145], v[144:145], 1.0 op_sel_hi:[1,0]
	v_rcp_f32_e32 v130, v130
	v_rcp_f32_e32 v131, v131
	v_rcp_f32_e32 v132, v132
	v_rcp_f32_e32 v133, v133
	v_rcp_f32_e32 v134, v134
	v_rcp_f32_e32 v135, v135
	v_rcp_f32_e32 v136, v136
	v_rcp_f32_e32 v137, v137
	v_rcp_f32_e32 v138, v138
	v_rcp_f32_e32 v139, v139
	v_rcp_f32_e32 v140, v140
	v_rcp_f32_e32 v141, v141
	v_rcp_f32_e32 v142, v142
	v_rcp_f32_e32 v143, v143
	v_rcp_f32_e32 v144, v144
	v_rcp_f32_e32 v145, v145
	v_pk_fma_f32 v[130:131], v[130:131], 2.0, 1.0 op_sel_hi:[1,0,0] neg_lo:[1,0,0] neg_hi:[1,0,0]
	v_pk_fma_f32 v[132:133], v[132:133], 2.0, 1.0 op_sel_hi:[1,0,0] neg_lo:[1,0,0] neg_hi:[1,0,0]
	v_pk_fma_f32 v[134:135], v[134:135], 2.0, 1.0 op_sel_hi:[1,0,0] neg_lo:[1,0,0] neg_hi:[1,0,0]
	v_pk_fma_f32 v[136:137], v[136:137], 2.0, 1.0 op_sel_hi:[1,0,0] neg_lo:[1,0,0] neg_hi:[1,0,0]
	v_pk_fma_f32 v[138:139], v[138:139], 2.0, 1.0 op_sel_hi:[1,0,0] neg_lo:[1,0,0] neg_hi:[1,0,0]
	v_pk_fma_f32 v[140:141], v[140:141], 2.0, 1.0 op_sel_hi:[1,0,0] neg_lo:[1,0,0] neg_hi:[1,0,0]
	v_pk_fma_f32 v[142:143], v[142:143], 2.0, 1.0 op_sel_hi:[1,0,0] neg_lo:[1,0,0] neg_hi:[1,0,0]
	v_pk_fma_f32 v[144:145], v[144:145], 2.0, 1.0 op_sel_hi:[1,0,0] neg_lo:[1,0,0] neg_hi:[1,0,0]
	v_cvt_pk_f16_f32 v146, v130, v131
	v_cvt_pk_f16_f32 v147, v132, v133
	v_cvt_pk_f16_f32 v148, v134, v135
	v_cvt_pk_f16_f32 v149, v136, v137
	v_cvt_pk_f16_f32 v150, v138, v139
	v_cvt_pk_f16_f32 v151, v140, v141
	v_cvt_pk_f16_f32 v152, v142, v143
	v_cvt_pk_f16_f32 v153, v144, v145
	s_nop 1
	v_permlane32_swap_b32_e32 v146, v148
	v_permlane32_swap_b32_e32 v147, v149
	v_permlane32_swap_b32_e32 v150, v152
	v_permlane32_swap_b32_e32 v151, v153
	global_store_dwordx4 v157, v[146:149], s[32:33] sc1
	global_store_dwordx4 v157, v[150:153], s[32:33] offset:1024 sc1
	s_add_u32 s32, s32, 0x10000
	s_addc_u32 s33, s33, 0
	s_waitcnt lgkmcnt(0)
	v_mfma_f32_32x32x16_f16 v[114:129], v[82:85], v[50:53], 0
	v_mfma_f32_32x32x16_f16 v[114:129], v[86:89], v[54:57], v[114:129]
	v_mfma_f32_32x32x16_f16 v[114:129], v[90:93], v[58:61], v[114:129]
	v_mfma_f32_32x32x16_f16 v[114:129], v[94:97], v[62:65], v[114:129]
	v_pk_fma_f32 v[130:131], v[98:99], s[4:5], v[66:67] op_sel_hi:[1,0,1]
	v_pk_fma_f32 v[132:133], v[100:101], s[4:5], v[68:69] op_sel_hi:[1,0,1]
	v_pk_fma_f32 v[134:135], v[102:103], s[4:5], v[70:71] op_sel_hi:[1,0,1]
	v_pk_fma_f32 v[136:137], v[104:105], s[4:5], v[72:73] op_sel_hi:[1,0,1]
	v_pk_fma_f32 v[138:139], v[106:107], s[4:5], v[74:75] op_sel_hi:[1,0,1]
	v_pk_fma_f32 v[140:141], v[108:109], s[4:5], v[76:77] op_sel_hi:[1,0,1]
	v_pk_fma_f32 v[142:143], v[110:111], s[4:5], v[78:79] op_sel_hi:[1,0,1]
	v_pk_fma_f32 v[144:145], v[112:113], s[4:5], v[80:81] op_sel_hi:[1,0,1]
	v_exp_f32_e32 v130, v130
	v_exp_f32_e32 v131, v131
	v_exp_f32_e32 v132, v132
	v_exp_f32_e32 v133, v133
	v_exp_f32_e32 v134, v134
	v_exp_f32_e32 v135, v135
	v_exp_f32_e32 v136, v136
	v_exp_f32_e32 v137, v137
	v_exp_f32_e32 v138, v138
	v_exp_f32_e32 v139, v139
	v_exp_f32_e32 v140, v140
	v_exp_f32_e32 v141, v141
	v_exp_f32_e32 v142, v142
	v_exp_f32_e32 v143, v143
	v_exp_f32_e32 v144, v144
	v_exp_f32_e32 v145, v145
	v_pk_add_f32 v[130:131], v[130:131], 1.0 op_sel_hi:[1,0]
	v_pk_add_f32 v[132:133], v[132:133], 1.0 op_sel_hi:[1,0]
	v_pk_add_f32 v[134:135], v[134:135], 1.0 op_sel_hi:[1,0]
	v_pk_add_f32 v[136:137], v[136:137], 1.0 op_sel_hi:[1,0]
	v_pk_add_f32 v[138:139], v[138:139], 1.0 op_sel_hi:[1,0]
	v_pk_add_f32 v[140:141], v[140:141], 1.0 op_sel_hi:[1,0]
	v_pk_add_f32 v[142:143], v[142:143], 1.0 op_sel_hi:[1,0]
	v_pk_add_f32 v[144:145], v[144:145], 1.0 op_sel_hi:[1,0]
	v_rcp_f32_e32 v130, v130
	v_rcp_f32_e32 v131, v131
	v_rcp_f32_e32 v132, v132
	v_rcp_f32_e32 v133, v133
	v_rcp_f32_e32 v134, v134
	v_rcp_f32_e32 v135, v135
	v_rcp_f32_e32 v136, v136
	v_rcp_f32_e32 v137, v137
	v_rcp_f32_e32 v138, v138
	v_rcp_f32_e32 v139, v139
	v_rcp_f32_e32 v140, v140
	v_rcp_f32_e32 v141, v141
	v_rcp_f32_e32 v142, v142
	v_rcp_f32_e32 v143, v143
	v_rcp_f32_e32 v144, v144
	v_rcp_f32_e32 v145, v145
	v_pk_fma_f32 v[130:131], v[130:131], 2.0, 1.0 op_sel_hi:[1,0,0] neg_lo:[1,0,0] neg_hi:[1,0,0]
	v_pk_fma_f32 v[132:133], v[132:133], 2.0, 1.0 op_sel_hi:[1,0,0] neg_lo:[1,0,0] neg_hi:[1,0,0]
	v_pk_fma_f32 v[134:135], v[134:135], 2.0, 1.0 op_sel_hi:[1,0,0] neg_lo:[1,0,0] neg_hi:[1,0,0]
	v_pk_fma_f32 v[136:137], v[136:137], 2.0, 1.0 op_sel_hi:[1,0,0] neg_lo:[1,0,0] neg_hi:[1,0,0]
	v_pk_fma_f32 v[138:139], v[138:139], 2.0, 1.0 op_sel_hi:[1,0,0] neg_lo:[1,0,0] neg_hi:[1,0,0]
	v_pk_fma_f32 v[140:141], v[140:141], 2.0, 1.0 op_sel_hi:[1,0,0] neg_lo:[1,0,0] neg_hi:[1,0,0]
	v_pk_fma_f32 v[142:143], v[142:143], 2.0, 1.0 op_sel_hi:[1,0,0] neg_lo:[1,0,0] neg_hi:[1,0,0]
	v_pk_fma_f32 v[144:145], v[144:145], 2.0, 1.0 op_sel_hi:[1,0,0] neg_lo:[1,0,0] neg_hi:[1,0,0]
	v_cvt_pk_f16_f32 v146, v130, v131
	v_cvt_pk_f16_f32 v147, v132, v133
	v_cvt_pk_f16_f32 v148, v134, v135
	v_cvt_pk_f16_f32 v149, v136, v137
	v_cvt_pk_f16_f32 v150, v138, v139
	v_cvt_pk_f16_f32 v151, v140, v141
	v_cvt_pk_f16_f32 v152, v142, v143
	v_cvt_pk_f16_f32 v153, v144, v145
	s_nop 1
	v_permlane32_swap_b32_e32 v146, v148
	v_permlane32_swap_b32_e32 v147, v149
	v_permlane32_swap_b32_e32 v150, v152
	v_permlane32_swap_b32_e32 v151, v153
	global_store_dwordx4 v157, v[146:149], s[32:33] sc1
	global_store_dwordx4 v157, v[150:153], s[32:33] offset:1024 sc1
	s_add_u32 s32, s32, 0x10000
	s_addc_u32 s33, s33, 0
	v_pk_fma_f32 v[130:131], v[114:115], s[4:5], v[66:67] op_sel_hi:[1,0,1]
	v_pk_fma_f32 v[132:133], v[116:117], s[4:5], v[68:69] op_sel_hi:[1,0,1]
	v_pk_fma_f32 v[134:135], v[118:119], s[4:5], v[70:71] op_sel_hi:[1,0,1]
	v_pk_fma_f32 v[136:137], v[120:121], s[4:5], v[72:73] op_sel_hi:[1,0,1]
	v_pk_fma_f32 v[138:139], v[122:123], s[4:5], v[74:75] op_sel_hi:[1,0,1]
	v_pk_fma_f32 v[140:141], v[124:125], s[4:5], v[76:77] op_sel_hi:[1,0,1]
	v_pk_fma_f32 v[142:143], v[126:127], s[4:5], v[78:79] op_sel_hi:[1,0,1]
	v_pk_fma_f32 v[144:145], v[128:129], s[4:5], v[80:81] op_sel_hi:[1,0,1]
	v_exp_f32_e32 v130, v130
	v_exp_f32_e32 v131, v131
	v_exp_f32_e32 v132, v132
	v_exp_f32_e32 v133, v133
	v_exp_f32_e32 v134, v134
	v_exp_f32_e32 v135, v135
	v_exp_f32_e32 v136, v136
	v_exp_f32_e32 v137, v137
	v_exp_f32_e32 v138, v138
	v_exp_f32_e32 v139, v139
	v_exp_f32_e32 v140, v140
	v_exp_f32_e32 v141, v141
	v_exp_f32_e32 v142, v142
	v_exp_f32_e32 v143, v143
	v_exp_f32_e32 v144, v144
	v_exp_f32_e32 v145, v145
	v_pk_add_f32 v[130:131], v[130:131], 1.0 op_sel_hi:[1,0]
	v_pk_add_f32 v[132:133], v[132:133], 1.0 op_sel_hi:[1,0]
	v_pk_add_f32 v[134:135], v[134:135], 1.0 op_sel_hi:[1,0]
	v_pk_add_f32 v[136:137], v[136:137], 1.0 op_sel_hi:[1,0]
	v_pk_add_f32 v[138:139], v[138:139], 1.0 op_sel_hi:[1,0]
	v_pk_add_f32 v[140:141], v[140:141], 1.0 op_sel_hi:[1,0]
	v_pk_add_f32 v[142:143], v[142:143], 1.0 op_sel_hi:[1,0]
	v_pk_add_f32 v[144:145], v[144:145], 1.0 op_sel_hi:[1,0]
	v_rcp_f32_e32 v130, v130
	v_rcp_f32_e32 v131, v131
	v_rcp_f32_e32 v132, v132
	v_rcp_f32_e32 v133, v133
	v_rcp_f32_e32 v134, v134
	v_rcp_f32_e32 v135, v135
	v_rcp_f32_e32 v136, v136
	v_rcp_f32_e32 v137, v137
	v_rcp_f32_e32 v138, v138
	v_rcp_f32_e32 v139, v139
	v_rcp_f32_e32 v140, v140
	v_rcp_f32_e32 v141, v141
	v_rcp_f32_e32 v142, v142
	v_rcp_f32_e32 v143, v143
	v_rcp_f32_e32 v144, v144
	v_rcp_f32_e32 v145, v145
	v_pk_fma_f32 v[130:131], v[130:131], 2.0, 1.0 op_sel_hi:[1,0,0] neg_lo:[1,0,0] neg_hi:[1,0,0]
	v_pk_fma_f32 v[132:133], v[132:133], 2.0, 1.0 op_sel_hi:[1,0,0] neg_lo:[1,0,0] neg_hi:[1,0,0]
	v_pk_fma_f32 v[134:135], v[134:135], 2.0, 1.0 op_sel_hi:[1,0,0] neg_lo:[1,0,0] neg_hi:[1,0,0]
	v_pk_fma_f32 v[136:137], v[136:137], 2.0, 1.0 op_sel_hi:[1,0,0] neg_lo:[1,0,0] neg_hi:[1,0,0]
	v_pk_fma_f32 v[138:139], v[138:139], 2.0, 1.0 op_sel_hi:[1,0,0] neg_lo:[1,0,0] neg_hi:[1,0,0]
	v_pk_fma_f32 v[140:141], v[140:141], 2.0, 1.0 op_sel_hi:[1,0,0] neg_lo:[1,0,0] neg_hi:[1,0,0]
	v_pk_fma_f32 v[142:143], v[142:143], 2.0, 1.0 op_sel_hi:[1,0,0] neg_lo:[1,0,0] neg_hi:[1,0,0]
	v_pk_fma_f32 v[144:145], v[144:145], 2.0, 1.0 op_sel_hi:[1,0,0] neg_lo:[1,0,0] neg_hi:[1,0,0]
	v_cvt_pk_f16_f32 v146, v130, v131
	v_cvt_pk_f16_f32 v147, v132, v133
	v_cvt_pk_f16_f32 v148, v134, v135
	v_cvt_pk_f16_f32 v149, v136, v137
	v_cvt_pk_f16_f32 v150, v138, v139
	v_cvt_pk_f16_f32 v151, v140, v141
	v_cvt_pk_f16_f32 v152, v142, v143
	v_cvt_pk_f16_f32 v153, v144, v145
	s_nop 1
	v_permlane32_swap_b32_e32 v146, v148
	v_permlane32_swap_b32_e32 v147, v149
	v_permlane32_swap_b32_e32 v150, v152
	v_permlane32_swap_b32_e32 v151, v153
	global_store_dwordx4 v157, v[146:149], s[32:33] sc1
	global_store_dwordx4 v157, v[150:153], s[32:33] offset:1024 sc1
	s_waitcnt vmcnt(11)
	v_cvt_pk_f16_f32 v168, v168, v169
	v_cvt_pk_f16_f32 v169, v170, v171
	ds_write_b64 v164, v[168:169] offset:0
	s_waitcnt vmcnt(10)
	v_cvt_pk_f16_f32 v172, v172, v173
	v_cvt_pk_f16_f32 v173, v174, v175
	ds_write_b64 v164, v[172:173] offset:64
	s_waitcnt vmcnt(9)
	v_cvt_pk_f16_f32 v176, v176, v177
	v_cvt_pk_f16_f32 v177, v178, v179
	ds_write_b64 v164, v[176:177] offset:128
	s_waitcnt vmcnt(8)
	v_cvt_pk_f16_f32 v180, v180, v181
	v_cvt_pk_f16_f32 v181, v182, v183
	ds_write_b64 v164, v[180:181] offset:192
	s_waitcnt lgkmcnt(0)
	s_barrier
	ds_read_b128 v[2:5], v166
	ds_read_b128 v[6:9], v166 offset:32
	ds_read_u16 v10, v167 offset:0
	ds_read_u16 v11, v167 offset:272
	ds_read_u16 v12, v167 offset:544
	ds_read_u16 v13, v167 offset:816
	ds_read_u16 v14, v167 offset:1088
	ds_read_u16 v15, v167 offset:1360
	ds_read_u16 v16, v167 offset:1632
	ds_read_u16 v17, v167 offset:1904
	s_waitcnt lgkmcnt(8)
	global_store_dwordx4 v157, v[2:5], s[36:37] sc1
	global_store_dwordx4 v157, v[6:9], s[36:37] offset:1024 sc1
	s_waitcnt lgkmcnt(0)
	v_lshl_or_b32 v10, v11, 16, v10
	v_lshl_or_b32 v11, v13, 16, v12
	v_lshl_or_b32 v12, v15, 16, v14
	v_lshl_or_b32 v13, v17, 16, v16
	global_store_dwordx4 v157, v[10:13], s[38:39] sc1
	ds_read_u16 v18, v167 offset:4352
	ds_read_u16 v19, v167 offset:4624
	ds_read_u16 v20, v167 offset:4896
	ds_read_u16 v21, v167 offset:5168
	ds_read_u16 v22, v167 offset:5440
	ds_read_u16 v23, v167 offset:5712
	ds_read_u16 v24, v167 offset:5984
	ds_read_u16 v25, v167 offset:6256
	s_waitcnt lgkmcnt(0)
	v_lshl_or_b32 v18, v19, 16, v18
	v_lshl_or_b32 v19, v21, 16, v20
	v_lshl_or_b32 v20, v23, 16, v22
	v_lshl_or_b32 v21, v25, 16, v24
	global_store_dwordx4 v157, v[18:21], s[38:39] offset:1024 sc1
	s_endpgm
